# rwkv pass B loop rewritten by hand: ks=1 hi/lo split issued under the ks=0 MFMAs, chains accumulate in place in the Q-tile registers, prefetch loads issued under the ks=1 MFMAs, saddr addressing
# speedup vs baseline: 1.0003x; 1.0003x over previous
.LBB0_897:
	s_andn2_b64 vcc, exec, s[0:1]
	s_cbranch_vccnz .LBB0_1532
	v_readlane_b32 s0, v252, 5
	v_readlane_b32 s1, v252, 6
	s_load_dwordx2 s[4:5], s[0:1], 0x140
	s_load_dwordx8 s[8:15], s[0:1], 0x48
	v_readlane_b32 s2, v252, 58
	v_readlane_b32 s3, v252, 59
	s_mov_b32 s3, s51
	s_waitcnt lgkmcnt(0)
	v_writelane_b32 v252, s8, 61
	s_nop 1
	v_writelane_b32 v253, s11, 0
	v_writelane_b32 v253, s12, 1
	v_writelane_b32 v253, s13, 2
	v_writelane_b32 v252, s9, 62
	v_writelane_b32 v253, s14, 3
	v_writelane_b32 v252, s10, 63
	v_writelane_b32 v253, s15, 4
	s_load_dwordx4 s[8:11], s[0:1], 0x68
	s_waitcnt lgkmcnt(0)
	v_writelane_b32 v253, s8, 5
	s_nop 1
	v_writelane_b32 v253, s9, 6
	v_writelane_b32 v253, s10, 7
	v_writelane_b32 v253, s11, 8
	s_load_dwordx4 s[8:11], s[0:1], 0xe0
	s_mov_b32 s0, s2
	v_writelane_b32 v252, s0, 58
	s_waitcnt lgkmcnt(0)
	v_writelane_b32 v253, s8, 9
	s_nop 1
	v_writelane_b32 v253, s9, 10
	v_writelane_b32 v253, s10, 11
	v_writelane_b32 v252, s1, 59
	s_lshl_b64 s[0:1], s[2:3], 2
	v_writelane_b32 v253, s11, 12
	s_add_u32 s0, s4, s0
	v_writelane_b32 v253, s4, 13
	s_addc_u32 s1, s5, s1
	s_add_u32 s0, s0, 0x52c0
	v_writelane_b32 v253, s5, 14
	s_addc_u32 s1, s1, 0
	v_writelane_b32 v253, s0, 15
	s_nop 1
	v_writelane_b32 v253, s1, 16
	v_readlane_b32 s0, v252, 0
	s_cmp_gt_i32 s0, 63
	s_cbranch_scc1 .LBB0_906
	v_mov_b32_e32 v2, v0
	s_nop 0
	v_readfirstlane_b32 s0, v2
	s_cmp_gt_u32 s0, 63
	s_cbranch_scc1 .LBB0_906
	v_readlane_b32 s4, v252, 0
	s_mov_b32 s0, s4
	s_mov_b32 s1, s4
	s_lshl_b32 s2, s0, 2
	s_and_b32 s2, s2, 16
	s_andn2_b32 s1, s1, 31
	s_or_b32 s1, s1, s2
	v_readlane_b32 s18, v253, 13
	v_readlane_b32 s19, v253, 14
	s_add_u32 s6, s18, 0x58834100
	s_addc_u32 s7, s19, 0
	s_ashr_i32 s5, s1, 4
	s_and_b32 s9, s0, 3
	s_mul_i32 s0, s5, 0x410
	s_mul_hi_i32 s3, s5, 0x410
	s_or_b32 s2, s0, s9
	s_lshl_b32 s0, s4, 7
	s_waitcnt vmcnt(0)
	v_mov_b32_e32 v85, v0
	s_and_b32 s4, s0, 0xc00
	s_lshl_b64 s[0:1], s[2:3], 15
	s_add_u32 s0, s6, s0
	v_and_b32_e32 v84, 63, v85
	s_addc_u32 s1, s7, s1
	v_and_b32_e32 v2, 63, v0
	v_lshlrev_b32_e32 v3, 4, v2
	v_add_u32_e32 v80, 0x1000, v3
	v_and_b32_e32 v81, 15, v2
	v_lshrrev_b32_e32 v230, 4, v2
	s_lshl_b32 s8, s4, 2
	s_add_u32 s8, s8, 0x4000
	v_lshlrev_b32_e32 v231, 8, v81
	v_lshl_add_u32 v231, v230, 4, v231
	v_add_u32_e32 v231, s8, v231
	s_lshl_b32 s8, s4, 1
	v_lshlrev_b32_e32 v240, 7, v81
	v_lshl_add_u32 v240, v230, 3, v240
	v_add_u32_e32 v240, s8, v240
	s_mul_i32 s8, s5, 0x1040000
	s_lshl_b32 s10, s9, 14
	s_add_u32 s8, s8, s10
	s_add_u32 s8, s8, 0x60a34100
	s_add_u32 s2, s18, s8
	s_addc_u32 s3, s19, 0
	s_mov_b64 s[16:17], s[0:1]
	s_mov_b64 s[12:13], s[0:1]
	global_load_dwordx4 v[4:7], v3, s[12:13]
	global_load_dwordx4 v[8:11], v3, s[12:13] offset:1024
	global_load_dwordx4 v[12:15], v3, s[12:13] offset:2048
	global_load_dwordx4 v[16:19], v3, s[12:13] offset:3072
	global_load_dwordx4 v[20:23], v80, s[12:13]
	global_load_dwordx4 v[24:27], v80, s[12:13] offset:1024
	global_load_dwordx4 v[28:31], v80, s[12:13] offset:2048
	global_load_dwordx4 v[32:35], v80, s[12:13] offset:3072
	global_load_dwordx4 v[36:39], v231, s[12:13]
	global_load_dwordx4 v[40:43], v231, s[12:13] offset:64
	global_load_dwordx4 v[44:47], v231, s[12:13] offset:128
	global_load_dwordx4 v[48:51], v231, s[12:13] offset:192
	s_add_u32 s12, s12, 0x20000
	s_addc_u32 s13, s13, 0
	global_load_dwordx4 v[52:55], v3, s[12:13]
	global_load_dwordx4 v[56:59], v3, s[12:13] offset:1024
	global_load_dwordx4 v[60:63], v3, s[12:13] offset:2048
	global_load_dwordx4 v[64:67], v3, s[12:13] offset:3072
	global_load_dwordx4 v[68:71], v80, s[12:13]
	global_load_dwordx4 v[72:75], v80, s[12:13] offset:1024
	global_load_dwordx4 v[76:79], v80, s[12:13] offset:2048
	global_load_dwordx4 v[84:87], v80, s[12:13] offset:3072
	global_load_dwordx4 v[88:91], v231, s[12:13]
	global_load_dwordx4 v[92:95], v231, s[12:13] offset:64
	global_load_dwordx4 v[96:99], v231, s[12:13] offset:128
	global_load_dwordx4 v[100:103], v231, s[12:13] offset:192
	s_add_u32 s12, s12, 0x20000
	s_addc_u32 s13, s13, 0
	global_load_dwordx4 v[104:107], v3, s[12:13]
	global_load_dwordx4 v[108:111], v3, s[12:13] offset:1024
	global_load_dwordx4 v[112:115], v3, s[12:13] offset:2048
	global_load_dwordx4 v[116:119], v3, s[12:13] offset:3072
	global_load_dwordx4 v[120:123], v80, s[12:13]
	global_load_dwordx4 v[124:127], v80, s[12:13] offset:1024
	global_load_dwordx4 v[128:131], v80, s[12:13] offset:2048
	global_load_dwordx4 v[132:135], v80, s[12:13] offset:3072
	global_load_dwordx4 v[136:139], v231, s[12:13]
	global_load_dwordx4 v[140:143], v231, s[12:13] offset:64
	global_load_dwordx4 v[144:147], v231, s[12:13] offset:128
	global_load_dwordx4 v[148:151], v231, s[12:13] offset:192
	s_add_u32 s12, s12, 0x20000
	s_addc_u32 s13, s13, 0
	global_load_dwordx4 v[152:155], v3, s[12:13]
	global_load_dwordx4 v[156:159], v3, s[12:13] offset:1024
	global_load_dwordx4 v[160:163], v3, s[12:13] offset:2048
	global_load_dwordx4 v[164:167], v3, s[12:13] offset:3072
	global_load_dwordx4 v[168:171], v80, s[12:13]
	global_load_dwordx4 v[172:175], v80, s[12:13] offset:1024
	global_load_dwordx4 v[176:179], v80, s[12:13] offset:2048
	global_load_dwordx4 v[180:183], v80, s[12:13] offset:3072
	global_load_dwordx4 v[184:187], v231, s[12:13]
	global_load_dwordx4 v[188:191], v231, s[12:13] offset:64
	global_load_dwordx4 v[192:195], v231, s[12:13] offset:128
	global_load_dwordx4 v[196:199], v231, s[12:13] offset:192
	s_add_u32 s12, s12, 0x20000
	s_addc_u32 s13, s13, 0
	s_mov_b32 s14, 4
	s_mov_b32 s10, 0
	v_mov_b32_e32 v200, 0
	v_mov_b32_e32 v201, 0
	v_mov_b32_e32 v202, 0
	v_mov_b32_e32 v203, 0
	v_mov_b32_e32 v204, 0
	v_mov_b32_e32 v205, 0
	v_mov_b32_e32 v206, 0
	v_mov_b32_e32 v207, 0
	v_mov_b32_e32 v208, 0
	v_mov_b32_e32 v209, 0
	v_mov_b32_e32 v210, 0
	v_mov_b32_e32 v211, 0
	v_mov_b32_e32 v212, 0
	v_mov_b32_e32 v213, 0
	v_mov_b32_e32 v214, 0
	v_mov_b32_e32 v215, 0
	s_waitcnt vmcnt(0)
.Lpb_loop:
	s_waitcnt vmcnt(48)
	v_cvt_pk_bf16_f32 v216, v200, v201
	v_cvt_pk_bf16_f32 v217, v202, v203
	v_cvt_pk_bf16_f32 v218, v204, v205
	v_cvt_pk_bf16_f32 v219, v206, v207
	v_lshlrev_b32_e32 v246, 16, v216
	v_and_b32_e32 v247, 0xffff0000, v216
	v_sub_f32_e32 v246, v200, v246
	v_sub_f32_e32 v247, v201, v247
	v_cvt_pk_bf16_f32 v220, v246, v247
	v_lshlrev_b32_e32 v248, 16, v217
	v_and_b32_e32 v249, 0xffff0000, v217
	v_sub_f32_e32 v248, v202, v248
	v_sub_f32_e32 v249, v203, v249
	v_cvt_pk_bf16_f32 v221, v248, v249
	v_lshlrev_b32_e32 v246, 16, v218
	v_and_b32_e32 v247, 0xffff0000, v218
	v_sub_f32_e32 v246, v204, v246
	v_sub_f32_e32 v247, v205, v247
	v_cvt_pk_bf16_f32 v222, v246, v247
	v_lshlrev_b32_e32 v248, 16, v219
	v_and_b32_e32 v249, 0xffff0000, v219
	v_sub_f32_e32 v248, v206, v248
	v_sub_f32_e32 v249, v207, v249
	v_cvt_pk_bf16_f32 v223, v248, v249
	global_store_dwordx2 v240, v[216:217], s[2:3]
	global_store_dwordx2 v240, v[218:219], s[2:3] offset:32
	v_mfma_f32_16x16x32_bf16 v[36:39], v[4:7], v[216:219], v[36:39]
	v_cvt_pk_bf16_f32 v232, v208, v209
	v_cvt_pk_bf16_f32 v233, v210, v211
	v_cvt_pk_bf16_f32 v234, v212, v213
	v_mfma_f32_16x16x32_bf16 v[40:43], v[12:15], v[216:219], v[40:43]
	v_cvt_pk_bf16_f32 v235, v214, v215
	v_lshlrev_b32_e32 v246, 16, v232
	v_and_b32_e32 v247, 0xffff0000, v232
	v_mfma_f32_16x16x32_bf16 v[44:47], v[20:23], v[216:219], v[44:47]
	v_sub_f32_e32 v246, v208, v246
	v_sub_f32_e32 v247, v209, v247
	v_cvt_pk_bf16_f32 v236, v246, v247
	v_mfma_f32_16x16x32_bf16 v[48:51], v[28:31], v[216:219], v[48:51]
	v_lshlrev_b32_e32 v248, 16, v233
	v_and_b32_e32 v249, 0xffff0000, v233
	v_sub_f32_e32 v248, v210, v248
	v_mfma_f32_16x16x32_bf16 v[36:39], v[4:7], v[220:223], v[36:39]
	v_sub_f32_e32 v249, v211, v249
	v_cvt_pk_bf16_f32 v237, v248, v249
	v_lshlrev_b32_e32 v246, 16, v234
	v_mfma_f32_16x16x32_bf16 v[40:43], v[12:15], v[220:223], v[40:43]
	v_and_b32_e32 v247, 0xffff0000, v234
	v_sub_f32_e32 v246, v212, v246
	v_sub_f32_e32 v247, v213, v247
	v_mfma_f32_16x16x32_bf16 v[44:47], v[20:23], v[220:223], v[44:47]
	v_cvt_pk_bf16_f32 v238, v246, v247
	v_lshlrev_b32_e32 v248, 16, v235
	v_and_b32_e32 v249, 0xffff0000, v235
	v_mfma_f32_16x16x32_bf16 v[48:51], v[28:31], v[220:223], v[48:51]
	v_sub_f32_e32 v248, v214, v248
	v_sub_f32_e32 v249, v215, v249
	v_cvt_pk_bf16_f32 v239, v248, v249
	global_store_dwordx2 v240, v[232:233], s[2:3] offset:64
	global_store_dwordx2 v240, v[234:235], s[2:3] offset:96
	s_min_u32 s15, s14, 0x103
	s_lshl_b32 s15, s15, 17
	s_add_u32 s12, s16, s15
	s_addc_u32 s13, s17, 0
	v_mfma_f32_16x16x32_bf16 v[36:39], v[8:11], v[232:235], v[36:39]
	global_load_dwordx4 v[4:7], v3, s[12:13]
	global_load_dwordx4 v[12:15], v3, s[12:13] offset:2048
	v_mfma_f32_16x16x32_bf16 v[40:43], v[16:19], v[232:235], v[40:43]
	global_load_dwordx4 v[20:23], v80, s[12:13]
	global_load_dwordx4 v[28:31], v80, s[12:13] offset:2048
	v_mfma_f32_16x16x32_bf16 v[200:203], v[8:11], v[236:239], v[36:39]
	s_add_i32 s14, s14, 1
	s_add_u32 s2, s2, 0x10000
	v_mfma_f32_16x16x32_bf16 v[204:207], v[16:19], v[236:239], v[40:43]
	s_addc_u32 s3, s3, 0
	global_load_dwordx4 v[8:11], v3, s[12:13] offset:1024
	v_mfma_f32_16x16x32_bf16 v[44:47], v[24:27], v[232:235], v[44:47]
	global_load_dwordx4 v[16:19], v3, s[12:13] offset:3072
	global_load_dwordx4 v[36:39], v231, s[12:13]
	v_mfma_f32_16x16x32_bf16 v[48:51], v[32:35], v[232:235], v[48:51]
	global_load_dwordx4 v[40:43], v231, s[12:13] offset:64
	v_mfma_f32_16x16x32_bf16 v[208:211], v[24:27], v[236:239], v[44:47]
	v_mfma_f32_16x16x32_bf16 v[212:215], v[32:35], v[236:239], v[48:51]
	global_load_dwordx4 v[24:27], v80, s[12:13] offset:1024
	global_load_dwordx4 v[32:35], v80, s[12:13] offset:3072
	s_nop 3
	global_load_dwordx4 v[44:47], v231, s[12:13] offset:128
	global_load_dwordx4 v[48:51], v231, s[12:13] offset:192
	s_waitcnt vmcnt(48)
	v_cvt_pk_bf16_f32 v216, v200, v201
	v_cvt_pk_bf16_f32 v217, v202, v203
	v_cvt_pk_bf16_f32 v218, v204, v205
	v_cvt_pk_bf16_f32 v219, v206, v207
	v_lshlrev_b32_e32 v246, 16, v216
	v_and_b32_e32 v247, 0xffff0000, v216
	v_sub_f32_e32 v246, v200, v246
	v_sub_f32_e32 v247, v201, v247
	v_cvt_pk_bf16_f32 v220, v246, v247
	v_lshlrev_b32_e32 v248, 16, v217
	v_and_b32_e32 v249, 0xffff0000, v217
	v_sub_f32_e32 v248, v202, v248
	v_sub_f32_e32 v249, v203, v249
	v_cvt_pk_bf16_f32 v221, v248, v249
	v_lshlrev_b32_e32 v246, 16, v218
	v_and_b32_e32 v247, 0xffff0000, v218
	v_sub_f32_e32 v246, v204, v246
	v_sub_f32_e32 v247, v205, v247
	v_cvt_pk_bf16_f32 v222, v246, v247
	v_lshlrev_b32_e32 v248, 16, v219
	v_and_b32_e32 v249, 0xffff0000, v219
	v_sub_f32_e32 v248, v206, v248
	v_sub_f32_e32 v249, v207, v249
	v_cvt_pk_bf16_f32 v223, v248, v249
	global_store_dwordx2 v240, v[216:217], s[2:3]
	global_store_dwordx2 v240, v[218:219], s[2:3] offset:32
	v_mfma_f32_16x16x32_bf16 v[88:91], v[52:55], v[216:219], v[88:91]
	v_cvt_pk_bf16_f32 v232, v208, v209
	v_cvt_pk_bf16_f32 v233, v210, v211
	v_cvt_pk_bf16_f32 v234, v212, v213
	v_mfma_f32_16x16x32_bf16 v[92:95], v[60:63], v[216:219], v[92:95]
	v_cvt_pk_bf16_f32 v235, v214, v215
	v_lshlrev_b32_e32 v246, 16, v232
	v_and_b32_e32 v247, 0xffff0000, v232
	v_mfma_f32_16x16x32_bf16 v[96:99], v[68:71], v[216:219], v[96:99]
	v_sub_f32_e32 v246, v208, v246
	v_sub_f32_e32 v247, v209, v247
	v_cvt_pk_bf16_f32 v236, v246, v247
	v_mfma_f32_16x16x32_bf16 v[100:103], v[76:79], v[216:219], v[100:103]
	v_lshlrev_b32_e32 v248, 16, v233
	v_and_b32_e32 v249, 0xffff0000, v233
	v_sub_f32_e32 v248, v210, v248
	v_mfma_f32_16x16x32_bf16 v[88:91], v[52:55], v[220:223], v[88:91]
	v_sub_f32_e32 v249, v211, v249
	v_cvt_pk_bf16_f32 v237, v248, v249
	v_lshlrev_b32_e32 v246, 16, v234
	v_mfma_f32_16x16x32_bf16 v[92:95], v[60:63], v[220:223], v[92:95]
	v_and_b32_e32 v247, 0xffff0000, v234
	v_sub_f32_e32 v246, v212, v246
	v_sub_f32_e32 v247, v213, v247
	v_mfma_f32_16x16x32_bf16 v[96:99], v[68:71], v[220:223], v[96:99]
	v_cvt_pk_bf16_f32 v238, v246, v247
	v_lshlrev_b32_e32 v248, 16, v235
	v_and_b32_e32 v249, 0xffff0000, v235
	v_mfma_f32_16x16x32_bf16 v[100:103], v[76:79], v[220:223], v[100:103]
	v_sub_f32_e32 v248, v214, v248
	v_sub_f32_e32 v249, v215, v249
	v_cvt_pk_bf16_f32 v239, v248, v249
	global_store_dwordx2 v240, v[232:233], s[2:3] offset:64
	global_store_dwordx2 v240, v[234:235], s[2:3] offset:96
	s_min_u32 s15, s14, 0x103
	s_lshl_b32 s15, s15, 17
	s_add_u32 s12, s16, s15
	s_addc_u32 s13, s17, 0
	v_mfma_f32_16x16x32_bf16 v[88:91], v[56:59], v[232:235], v[88:91]
	global_load_dwordx4 v[52:55], v3, s[12:13]
	global_load_dwordx4 v[60:63], v3, s[12:13] offset:2048
	v_mfma_f32_16x16x32_bf16 v[92:95], v[64:67], v[232:235], v[92:95]
	global_load_dwordx4 v[68:71], v80, s[12:13]
	global_load_dwordx4 v[76:79], v80, s[12:13] offset:2048
	v_mfma_f32_16x16x32_bf16 v[200:203], v[56:59], v[236:239], v[88:91]
	s_add_i32 s14, s14, 1
	s_add_u32 s2, s2, 0x10000
	v_mfma_f32_16x16x32_bf16 v[204:207], v[64:67], v[236:239], v[92:95]
	s_addc_u32 s3, s3, 0
	global_load_dwordx4 v[56:59], v3, s[12:13] offset:1024
	v_mfma_f32_16x16x32_bf16 v[96:99], v[72:75], v[232:235], v[96:99]
	global_load_dwordx4 v[64:67], v3, s[12:13] offset:3072
	global_load_dwordx4 v[88:91], v231, s[12:13]
	v_mfma_f32_16x16x32_bf16 v[100:103], v[84:87], v[232:235], v[100:103]
	global_load_dwordx4 v[92:95], v231, s[12:13] offset:64
	v_mfma_f32_16x16x32_bf16 v[208:211], v[72:75], v[236:239], v[96:99]
	v_mfma_f32_16x16x32_bf16 v[212:215], v[84:87], v[236:239], v[100:103]
	global_load_dwordx4 v[72:75], v80, s[12:13] offset:1024
	global_load_dwordx4 v[84:87], v80, s[12:13] offset:3072
	s_nop 3
	global_load_dwordx4 v[96:99], v231, s[12:13] offset:128
	global_load_dwordx4 v[100:103], v231, s[12:13] offset:192
	s_waitcnt vmcnt(48)
	v_cvt_pk_bf16_f32 v216, v200, v201
	v_cvt_pk_bf16_f32 v217, v202, v203
	v_cvt_pk_bf16_f32 v218, v204, v205
	v_cvt_pk_bf16_f32 v219, v206, v207
	v_lshlrev_b32_e32 v246, 16, v216
	v_and_b32_e32 v247, 0xffff0000, v216
	v_sub_f32_e32 v246, v200, v246
	v_sub_f32_e32 v247, v201, v247
	v_cvt_pk_bf16_f32 v220, v246, v247
	v_lshlrev_b32_e32 v248, 16, v217
	v_and_b32_e32 v249, 0xffff0000, v217
	v_sub_f32_e32 v248, v202, v248
	v_sub_f32_e32 v249, v203, v249
	v_cvt_pk_bf16_f32 v221, v248, v249
	v_lshlrev_b32_e32 v246, 16, v218
	v_and_b32_e32 v247, 0xffff0000, v218
	v_sub_f32_e32 v246, v204, v246
	v_sub_f32_e32 v247, v205, v247
	v_cvt_pk_bf16_f32 v222, v246, v247
	v_lshlrev_b32_e32 v248, 16, v219
	v_and_b32_e32 v249, 0xffff0000, v219
	v_sub_f32_e32 v248, v206, v248
	v_sub_f32_e32 v249, v207, v249
	v_cvt_pk_bf16_f32 v223, v248, v249
	global_store_dwordx2 v240, v[216:217], s[2:3]
	global_store_dwordx2 v240, v[218:219], s[2:3] offset:32
	v_mfma_f32_16x16x32_bf16 v[136:139], v[104:107], v[216:219], v[136:139]
	v_cvt_pk_bf16_f32 v232, v208, v209
	v_cvt_pk_bf16_f32 v233, v210, v211
	v_cvt_pk_bf16_f32 v234, v212, v213
	v_mfma_f32_16x16x32_bf16 v[140:143], v[112:115], v[216:219], v[140:143]
	v_cvt_pk_bf16_f32 v235, v214, v215
	v_lshlrev_b32_e32 v246, 16, v232
	v_and_b32_e32 v247, 0xffff0000, v232
	v_mfma_f32_16x16x32_bf16 v[144:147], v[120:123], v[216:219], v[144:147]
	v_sub_f32_e32 v246, v208, v246
	v_sub_f32_e32 v247, v209, v247
	v_cvt_pk_bf16_f32 v236, v246, v247
	v_mfma_f32_16x16x32_bf16 v[148:151], v[128:131], v[216:219], v[148:151]
	v_lshlrev_b32_e32 v248, 16, v233
	v_and_b32_e32 v249, 0xffff0000, v233
	v_sub_f32_e32 v248, v210, v248
	v_mfma_f32_16x16x32_bf16 v[136:139], v[104:107], v[220:223], v[136:139]
	v_sub_f32_e32 v249, v211, v249
	v_cvt_pk_bf16_f32 v237, v248, v249
	v_lshlrev_b32_e32 v246, 16, v234
	v_mfma_f32_16x16x32_bf16 v[140:143], v[112:115], v[220:223], v[140:143]
	v_and_b32_e32 v247, 0xffff0000, v234
	v_sub_f32_e32 v246, v212, v246
	v_sub_f32_e32 v247, v213, v247
	v_mfma_f32_16x16x32_bf16 v[144:147], v[120:123], v[220:223], v[144:147]
	v_cvt_pk_bf16_f32 v238, v246, v247
	v_lshlrev_b32_e32 v248, 16, v235
	v_and_b32_e32 v249, 0xffff0000, v235
	v_mfma_f32_16x16x32_bf16 v[148:151], v[128:131], v[220:223], v[148:151]
	v_sub_f32_e32 v248, v214, v248
	v_sub_f32_e32 v249, v215, v249
	v_cvt_pk_bf16_f32 v239, v248, v249
	global_store_dwordx2 v240, v[232:233], s[2:3] offset:64
	global_store_dwordx2 v240, v[234:235], s[2:3] offset:96
	s_min_u32 s15, s14, 0x103
	s_lshl_b32 s15, s15, 17
	s_add_u32 s12, s16, s15
	s_addc_u32 s13, s17, 0
	v_mfma_f32_16x16x32_bf16 v[136:139], v[108:111], v[232:235], v[136:139]
	global_load_dwordx4 v[104:107], v3, s[12:13]
	global_load_dwordx4 v[112:115], v3, s[12:13] offset:2048
	v_mfma_f32_16x16x32_bf16 v[140:143], v[116:119], v[232:235], v[140:143]
	global_load_dwordx4 v[120:123], v80, s[12:13]
	global_load_dwordx4 v[128:131], v80, s[12:13] offset:2048
	v_mfma_f32_16x16x32_bf16 v[200:203], v[108:111], v[236:239], v[136:139]
	s_add_i32 s14, s14, 1
	s_add_u32 s2, s2, 0x10000
	v_mfma_f32_16x16x32_bf16 v[204:207], v[116:119], v[236:239], v[140:143]
	s_addc_u32 s3, s3, 0
	global_load_dwordx4 v[108:111], v3, s[12:13] offset:1024
	v_mfma_f32_16x16x32_bf16 v[144:147], v[124:127], v[232:235], v[144:147]
	global_load_dwordx4 v[116:119], v3, s[12:13] offset:3072
	global_load_dwordx4 v[136:139], v231, s[12:13]
	v_mfma_f32_16x16x32_bf16 v[148:151], v[132:135], v[232:235], v[148:151]
	global_load_dwordx4 v[140:143], v231, s[12:13] offset:64
	v_mfma_f32_16x16x32_bf16 v[208:211], v[124:127], v[236:239], v[144:147]
	v_mfma_f32_16x16x32_bf16 v[212:215], v[132:135], v[236:239], v[148:151]
	global_load_dwordx4 v[124:127], v80, s[12:13] offset:1024
	global_load_dwordx4 v[132:135], v80, s[12:13] offset:3072
	s_nop 3
	global_load_dwordx4 v[144:147], v231, s[12:13] offset:128
	global_load_dwordx4 v[148:151], v231, s[12:13] offset:192
	s_waitcnt vmcnt(48)
	v_cvt_pk_bf16_f32 v216, v200, v201
	v_cvt_pk_bf16_f32 v217, v202, v203
	v_cvt_pk_bf16_f32 v218, v204, v205
	v_cvt_pk_bf16_f32 v219, v206, v207
	v_lshlrev_b32_e32 v246, 16, v216
	v_and_b32_e32 v247, 0xffff0000, v216
	v_sub_f32_e32 v246, v200, v246
	v_sub_f32_e32 v247, v201, v247
	v_cvt_pk_bf16_f32 v220, v246, v247
	v_lshlrev_b32_e32 v248, 16, v217
	v_and_b32_e32 v249, 0xffff0000, v217
	v_sub_f32_e32 v248, v202, v248
	v_sub_f32_e32 v249, v203, v249
	v_cvt_pk_bf16_f32 v221, v248, v249
	v_lshlrev_b32_e32 v246, 16, v218
	v_and_b32_e32 v247, 0xffff0000, v218
	v_sub_f32_e32 v246, v204, v246
	v_sub_f32_e32 v247, v205, v247
	v_cvt_pk_bf16_f32 v222, v246, v247
	v_lshlrev_b32_e32 v248, 16, v219
	v_and_b32_e32 v249, 0xffff0000, v219
	v_sub_f32_e32 v248, v206, v248
	v_sub_f32_e32 v249, v207, v249
	v_cvt_pk_bf16_f32 v223, v248, v249
	global_store_dwordx2 v240, v[216:217], s[2:3]
	global_store_dwordx2 v240, v[218:219], s[2:3] offset:32
	v_mfma_f32_16x16x32_bf16 v[184:187], v[152:155], v[216:219], v[184:187]
	v_cvt_pk_bf16_f32 v232, v208, v209
	v_cvt_pk_bf16_f32 v233, v210, v211
	v_cvt_pk_bf16_f32 v234, v212, v213
	v_mfma_f32_16x16x32_bf16 v[188:191], v[160:163], v[216:219], v[188:191]
	v_cvt_pk_bf16_f32 v235, v214, v215
	v_lshlrev_b32_e32 v246, 16, v232
	v_and_b32_e32 v247, 0xffff0000, v232
	v_mfma_f32_16x16x32_bf16 v[192:195], v[168:171], v[216:219], v[192:195]
	v_sub_f32_e32 v246, v208, v246
	v_sub_f32_e32 v247, v209, v247
	v_cvt_pk_bf16_f32 v236, v246, v247
	v_mfma_f32_16x16x32_bf16 v[196:199], v[176:179], v[216:219], v[196:199]
	v_lshlrev_b32_e32 v248, 16, v233
	v_and_b32_e32 v249, 0xffff0000, v233
	v_sub_f32_e32 v248, v210, v248
	v_mfma_f32_16x16x32_bf16 v[184:187], v[152:155], v[220:223], v[184:187]
	v_sub_f32_e32 v249, v211, v249
	v_cvt_pk_bf16_f32 v237, v248, v249
	v_lshlrev_b32_e32 v246, 16, v234
	v_mfma_f32_16x16x32_bf16 v[188:191], v[160:163], v[220:223], v[188:191]
	v_and_b32_e32 v247, 0xffff0000, v234
	v_sub_f32_e32 v246, v212, v246
	v_sub_f32_e32 v247, v213, v247
	v_mfma_f32_16x16x32_bf16 v[192:195], v[168:171], v[220:223], v[192:195]
	v_cvt_pk_bf16_f32 v238, v246, v247
	v_lshlrev_b32_e32 v248, 16, v235
	v_and_b32_e32 v249, 0xffff0000, v235
	v_mfma_f32_16x16x32_bf16 v[196:199], v[176:179], v[220:223], v[196:199]
	v_sub_f32_e32 v248, v214, v248
	v_sub_f32_e32 v249, v215, v249
	v_cvt_pk_bf16_f32 v239, v248, v249
	global_store_dwordx2 v240, v[232:233], s[2:3] offset:64
	global_store_dwordx2 v240, v[234:235], s[2:3] offset:96
	s_min_u32 s15, s14, 0x103
	s_lshl_b32 s15, s15, 17
	s_add_u32 s12, s16, s15
	s_addc_u32 s13, s17, 0
	v_mfma_f32_16x16x32_bf16 v[184:187], v[156:159], v[232:235], v[184:187]
	global_load_dwordx4 v[152:155], v3, s[12:13]
	global_load_dwordx4 v[160:163], v3, s[12:13] offset:2048
	v_mfma_f32_16x16x32_bf16 v[188:191], v[164:167], v[232:235], v[188:191]
	global_load_dwordx4 v[168:171], v80, s[12:13]
	global_load_dwordx4 v[176:179], v80, s[12:13] offset:2048
	v_mfma_f32_16x16x32_bf16 v[200:203], v[156:159], v[236:239], v[184:187]
	s_add_i32 s14, s14, 1
	s_add_u32 s2, s2, 0x10000
	v_mfma_f32_16x16x32_bf16 v[204:207], v[164:167], v[236:239], v[188:191]
	s_addc_u32 s3, s3, 0
	global_load_dwordx4 v[156:159], v3, s[12:13] offset:1024
	v_mfma_f32_16x16x32_bf16 v[192:195], v[172:175], v[232:235], v[192:195]
	global_load_dwordx4 v[164:167], v3, s[12:13] offset:3072
	global_load_dwordx4 v[184:187], v231, s[12:13]
	v_mfma_f32_16x16x32_bf16 v[196:199], v[180:183], v[232:235], v[196:199]
	global_load_dwordx4 v[188:191], v231, s[12:13] offset:64
	v_mfma_f32_16x16x32_bf16 v[208:211], v[172:175], v[236:239], v[192:195]
	v_mfma_f32_16x16x32_bf16 v[212:215], v[180:183], v[236:239], v[196:199]
	global_load_dwordx4 v[172:175], v80, s[12:13] offset:1024
	global_load_dwordx4 v[180:183], v80, s[12:13] offset:3072
	s_nop 3
	global_load_dwordx4 v[192:195], v231, s[12:13] offset:128
	global_load_dwordx4 v[196:199], v231, s[12:13] offset:192
	s_add_i32 s10, s10, 4
	s_cmpk_lt_u32 s10, 0x104
	s_cbranch_scc1 .Lpb_loop
	s_nop 0
	s_nop 0
	s_nop 0
	s_nop 0
	s_nop 0
	s_nop 0
	s_nop 0
	s_nop 0
	s_nop 0
	s_nop 0
	s_nop 0
	s_nop 0
	s_nop 0
	s_nop 0
	s_nop 0
	s_waitcnt vmcnt(30)
	v_mov_b32_e32 v2, v0
	s_waitcnt vmcnt(0)
	buffer_wbl2 sc1
	s_waitcnt vmcnt(0)
	s_waitcnt vmcnt(0)
	s_nop 0
	v_and_b32_e32 v2, 63, v2
	v_cmp_eq_u32_e32 vcc, 0, v2
	s_and_saveexec_b64 s[0:1], vcc
	s_cbranch_execz .LBB0_905
	s_mov_b64 s[2:3], exec
	v_mbcnt_lo_u32_b32 v2, s2, 0
	v_mbcnt_hi_u32_b32 v2, s3, v2
	v_cmp_eq_u32_e32 vcc, 0, v2
	s_and_b64 s[4:5], exec, vcc
	s_mov_b64 exec, s[4:5]
	s_cbranch_execz .LBB0_905
	s_bcnt1_i32_b64 s2, s[2:3]
	v_mov_b32_e32 v2, s2
	v_readlane_b32 s2, v253, 15
	v_readlane_b32 s3, v253, 16
	s_nop 4
	global_atomic_add v83, v2, s[2:3]
